# prologue adaLN GEMV loop unrolled with weight loads two k-groups ahead (3 rotating register sets)
# baseline (speedup 1.0000x reference)
.LBB0_119:
	s_mov_b32 s9, 0
	s_mov_b32 s5, 0
	s_mov_b32 s8, 0x0
	v_lshl_add_u64 v[226:227], v[30:31], 0, s[8:9]
	s_add_u32 s4, s8, s12
	v_lshl_add_u64 v[228:229], v[30:31], 0, s[4:5]
	global_load_dwordx4 v[34:37], v[226:227], off
	s_add_u32 s4, s8, s13
	v_lshl_add_u64 v[230:231], v[30:31], 0, s[4:5]
	global_load_dwordx4 v[38:41], v[228:229], off
	s_add_u32 s4, s8, s14
	v_lshl_add_u64 v[232:233], v[30:31], 0, s[4:5]
	global_load_dwordx4 v[42:45], v[230:231], off
	global_load_dwordx4 v[46:49], v[232:233], off
	s_mov_b32 s8, 0x300000
	v_lshl_add_u64 v[226:227], v[30:31], 0, s[8:9]
	s_add_u32 s4, s8, s12
	v_lshl_add_u64 v[228:229], v[30:31], 0, s[4:5]
	global_load_dwordx4 v[192:195], v[226:227], off
	s_add_u32 s4, s8, s13
	v_lshl_add_u64 v[230:231], v[30:31], 0, s[4:5]
	global_load_dwordx4 v[196:199], v[228:229], off
	s_add_u32 s4, s8, s14
	v_lshl_add_u64 v[232:233], v[30:31], 0, s[4:5]
	global_load_dwordx4 v[200:203], v[230:231], off
	global_load_dwordx4 v[204:207], v[232:233], off
	s_mov_b32 s8, 0x600000
	v_lshl_add_u64 v[226:227], v[30:31], 0, s[8:9]
	s_add_u32 s4, s8, s12
	v_lshl_add_u64 v[228:229], v[30:31], 0, s[4:5]
	global_load_dwordx4 v[208:211], v[226:227], off
	s_add_u32 s4, s8, s13
	v_lshl_add_u64 v[230:231], v[30:31], 0, s[4:5]
	global_load_dwordx4 v[212:215], v[228:229], off
	s_add_u32 s4, s8, s14
	v_lshl_add_u64 v[232:233], v[30:31], 0, s[4:5]
	global_load_dwordx4 v[216:219], v[230:231], off
	global_load_dwordx4 v[220:223], v[232:233], off
	v_add_u32_e32 v33, 0x1000, v26
	v_add_u32_e32 v64, 0x2000, v26
	ds_read2_b32 v[50:51], v26 offset1:32
	v_add_u32_e32 v66, 0x3000, v26
	v_add_u32_e32 v68, 0x4000, v26
	ds_read2_b32 v[52:53], v26 offset0:64 offset1:96
	ds_read2_b32 v[54:55], v33 offset1:32
	ds_read2_b32 v[56:57], v64 offset1:32
	ds_read2_b32 v[58:59], v66 offset1:32
	ds_read2_b32 v[60:61], v68 offset1:32
	ds_read2_b32 v[62:63], v33 offset0:64 offset1:96
	ds_read2_b32 v[64:65], v64 offset0:64 offset1:96
	ds_read2_b32 v[66:67], v66 offset0:64 offset1:96
	ds_read2_b32 v[68:69], v68 offset0:64 offset1:96
	s_waitcnt lgkmcnt(9)
	v_mov_b32_e32 v70, v51
	s_waitcnt lgkmcnt(7)
	v_mov_b32_e32 v74, v55
	s_waitcnt lgkmcnt(6)
	v_mov_b32_e32 v76, v57
	s_waitcnt lgkmcnt(5)
	v_mov_b32_e32 v78, v59
	s_waitcnt lgkmcnt(4)
	v_mov_b32_e32 v80, v61
	v_mov_b32_e32 v72, v53
	s_waitcnt lgkmcnt(3)
	v_mov_b32_e32 v82, v63
	s_waitcnt lgkmcnt(2)
	v_mov_b32_e32 v84, v65
	s_waitcnt lgkmcnt(1)
	v_mov_b32_e32 v86, v67
	s_waitcnt lgkmcnt(0)
	v_mov_b32_e32 v88, v69
	v_add_u32_e32 v26, 0x200, v26
	s_waitcnt vmcnt(11)
	v_pk_fma_f32 v[18:19], v[34:35], v[50:51], v[18:19] op_sel_hi:[1,0,1]
	v_pk_fma_f32 v[20:21], v[36:37], v[50:51], v[20:21] op_sel_hi:[1,0,1]
	v_pk_fma_f32 v[14:15], v[34:35], v[54:55], v[14:15] op_sel_hi:[1,0,1]
	v_pk_fma_f32 v[16:17], v[36:37], v[54:55], v[16:17] op_sel_hi:[1,0,1]
	v_pk_fma_f32 v[10:11], v[34:35], v[56:57], v[10:11] op_sel_hi:[1,0,1]
	v_pk_fma_f32 v[12:13], v[36:37], v[56:57], v[12:13] op_sel_hi:[1,0,1]
	v_pk_fma_f32 v[6:7], v[34:35], v[58:59], v[6:7] op_sel_hi:[1,0,1]
	v_pk_fma_f32 v[8:9], v[36:37], v[58:59], v[8:9] op_sel_hi:[1,0,1]
	v_pk_fma_f32 v[2:3], v[34:35], v[60:61], v[2:3] op_sel_hi:[1,0,1]
	v_pk_fma_f32 v[4:5], v[36:37], v[60:61], v[4:5] op_sel_hi:[1,0,1]
	s_waitcnt vmcnt(10)
	v_pk_fma_f32 v[18:19], v[38:39], v[70:71], v[18:19] op_sel_hi:[1,0,1]
	v_pk_fma_f32 v[20:21], v[40:41], v[70:71], v[20:21] op_sel_hi:[1,0,1]
	v_pk_fma_f32 v[14:15], v[38:39], v[74:75], v[14:15] op_sel_hi:[1,0,1]
	v_pk_fma_f32 v[16:17], v[40:41], v[74:75], v[16:17] op_sel_hi:[1,0,1]
	v_pk_fma_f32 v[10:11], v[38:39], v[76:77], v[10:11] op_sel_hi:[1,0,1]
	v_pk_fma_f32 v[12:13], v[40:41], v[76:77], v[12:13] op_sel_hi:[1,0,1]
	v_pk_fma_f32 v[6:7], v[38:39], v[78:79], v[6:7] op_sel_hi:[1,0,1]
	v_pk_fma_f32 v[8:9], v[40:41], v[78:79], v[8:9] op_sel_hi:[1,0,1]
	v_pk_fma_f32 v[2:3], v[38:39], v[80:81], v[2:3] op_sel_hi:[1,0,1]
	v_pk_fma_f32 v[4:5], v[40:41], v[80:81], v[4:5] op_sel_hi:[1,0,1]
	s_waitcnt vmcnt(9)
	v_pk_fma_f32 v[18:19], v[42:43], v[52:53], v[18:19] op_sel_hi:[1,0,1]
	v_pk_fma_f32 v[20:21], v[44:45], v[52:53], v[20:21] op_sel_hi:[1,0,1]
	v_pk_fma_f32 v[14:15], v[42:43], v[62:63], v[14:15] op_sel_hi:[1,0,1]
	v_pk_fma_f32 v[16:17], v[44:45], v[62:63], v[16:17] op_sel_hi:[1,0,1]
	v_pk_fma_f32 v[10:11], v[42:43], v[64:65], v[10:11] op_sel_hi:[1,0,1]
	v_pk_fma_f32 v[12:13], v[44:45], v[64:65], v[12:13] op_sel_hi:[1,0,1]
	v_pk_fma_f32 v[6:7], v[42:43], v[66:67], v[6:7] op_sel_hi:[1,0,1]
	v_pk_fma_f32 v[8:9], v[44:45], v[66:67], v[8:9] op_sel_hi:[1,0,1]
	v_pk_fma_f32 v[2:3], v[42:43], v[68:69], v[2:3] op_sel_hi:[1,0,1]
	v_pk_fma_f32 v[4:5], v[44:45], v[68:69], v[4:5] op_sel_hi:[1,0,1]
	s_waitcnt vmcnt(8)
	v_pk_fma_f32 v[18:19], v[46:47], v[72:73], v[18:19] op_sel_hi:[1,0,1]
	v_pk_fma_f32 v[20:21], v[48:49], v[72:73], v[20:21] op_sel_hi:[1,0,1]
	v_pk_fma_f32 v[14:15], v[46:47], v[82:83], v[14:15] op_sel_hi:[1,0,1]
	v_pk_fma_f32 v[16:17], v[48:49], v[82:83], v[16:17] op_sel_hi:[1,0,1]
	v_pk_fma_f32 v[10:11], v[46:47], v[84:85], v[10:11] op_sel_hi:[1,0,1]
	v_pk_fma_f32 v[12:13], v[48:49], v[84:85], v[12:13] op_sel_hi:[1,0,1]
	v_pk_fma_f32 v[6:7], v[46:47], v[86:87], v[6:7] op_sel_hi:[1,0,1]
	v_pk_fma_f32 v[8:9], v[48:49], v[86:87], v[8:9] op_sel_hi:[1,0,1]
	v_pk_fma_f32 v[2:3], v[46:47], v[88:89], v[2:3] op_sel_hi:[1,0,1]
	v_pk_fma_f32 v[4:5], v[48:49], v[88:89], v[4:5] op_sel_hi:[1,0,1]
	s_mov_b32 s8, 0x900000
	v_lshl_add_u64 v[226:227], v[30:31], 0, s[8:9]
	s_add_u32 s4, s8, s12
	v_lshl_add_u64 v[228:229], v[30:31], 0, s[4:5]
	global_load_dwordx4 v[34:37], v[226:227], off
	s_add_u32 s4, s8, s13
	v_lshl_add_u64 v[230:231], v[30:31], 0, s[4:5]
	global_load_dwordx4 v[38:41], v[228:229], off
	s_add_u32 s4, s8, s14
	v_lshl_add_u64 v[232:233], v[30:31], 0, s[4:5]
	global_load_dwordx4 v[42:45], v[230:231], off
	global_load_dwordx4 v[46:49], v[232:233], off
	v_add_u32_e32 v33, 0x1000, v26
	v_add_u32_e32 v64, 0x2000, v26
	ds_read2_b32 v[50:51], v26 offset1:32
	v_add_u32_e32 v66, 0x3000, v26
	v_add_u32_e32 v68, 0x4000, v26
	ds_read2_b32 v[52:53], v26 offset0:64 offset1:96
	ds_read2_b32 v[54:55], v33 offset1:32
	ds_read2_b32 v[56:57], v64 offset1:32
	ds_read2_b32 v[58:59], v66 offset1:32
	ds_read2_b32 v[60:61], v68 offset1:32
	ds_read2_b32 v[62:63], v33 offset0:64 offset1:96
	ds_read2_b32 v[64:65], v64 offset0:64 offset1:96
	ds_read2_b32 v[66:67], v66 offset0:64 offset1:96
	ds_read2_b32 v[68:69], v68 offset0:64 offset1:96
	s_waitcnt lgkmcnt(9)
	v_mov_b32_e32 v70, v51
	s_waitcnt lgkmcnt(7)
	v_mov_b32_e32 v74, v55
	s_waitcnt lgkmcnt(6)
	v_mov_b32_e32 v76, v57
	s_waitcnt lgkmcnt(5)
	v_mov_b32_e32 v78, v59
	s_waitcnt lgkmcnt(4)
	v_mov_b32_e32 v80, v61
	v_mov_b32_e32 v72, v53
	s_waitcnt lgkmcnt(3)
	v_mov_b32_e32 v82, v63
	s_waitcnt lgkmcnt(2)
	v_mov_b32_e32 v84, v65
	s_waitcnt lgkmcnt(1)
	v_mov_b32_e32 v86, v67
	s_waitcnt lgkmcnt(0)
	v_mov_b32_e32 v88, v69
	v_add_u32_e32 v26, 0x200, v26
	s_waitcnt vmcnt(11)
	v_pk_fma_f32 v[18:19], v[192:193], v[50:51], v[18:19] op_sel_hi:[1,0,1]
	v_pk_fma_f32 v[20:21], v[194:195], v[50:51], v[20:21] op_sel_hi:[1,0,1]
	v_pk_fma_f32 v[14:15], v[192:193], v[54:55], v[14:15] op_sel_hi:[1,0,1]
	v_pk_fma_f32 v[16:17], v[194:195], v[54:55], v[16:17] op_sel_hi:[1,0,1]
	v_pk_fma_f32 v[10:11], v[192:193], v[56:57], v[10:11] op_sel_hi:[1,0,1]
	v_pk_fma_f32 v[12:13], v[194:195], v[56:57], v[12:13] op_sel_hi:[1,0,1]
	v_pk_fma_f32 v[6:7], v[192:193], v[58:59], v[6:7] op_sel_hi:[1,0,1]
	v_pk_fma_f32 v[8:9], v[194:195], v[58:59], v[8:9] op_sel_hi:[1,0,1]
	v_pk_fma_f32 v[2:3], v[192:193], v[60:61], v[2:3] op_sel_hi:[1,0,1]
	v_pk_fma_f32 v[4:5], v[194:195], v[60:61], v[4:5] op_sel_hi:[1,0,1]
	s_waitcnt vmcnt(10)
	v_pk_fma_f32 v[18:19], v[196:197], v[70:71], v[18:19] op_sel_hi:[1,0,1]
	v_pk_fma_f32 v[20:21], v[198:199], v[70:71], v[20:21] op_sel_hi:[1,0,1]
	v_pk_fma_f32 v[14:15], v[196:197], v[74:75], v[14:15] op_sel_hi:[1,0,1]
	v_pk_fma_f32 v[16:17], v[198:199], v[74:75], v[16:17] op_sel_hi:[1,0,1]
	v_pk_fma_f32 v[10:11], v[196:197], v[76:77], v[10:11] op_sel_hi:[1,0,1]
	v_pk_fma_f32 v[12:13], v[198:199], v[76:77], v[12:13] op_sel_hi:[1,0,1]
	v_pk_fma_f32 v[6:7], v[196:197], v[78:79], v[6:7] op_sel_hi:[1,0,1]
	v_pk_fma_f32 v[8:9], v[198:199], v[78:79], v[8:9] op_sel_hi:[1,0,1]
	v_pk_fma_f32 v[2:3], v[196:197], v[80:81], v[2:3] op_sel_hi:[1,0,1]
	v_pk_fma_f32 v[4:5], v[198:199], v[80:81], v[4:5] op_sel_hi:[1,0,1]
	s_waitcnt vmcnt(9)
	v_pk_fma_f32 v[18:19], v[200:201], v[52:53], v[18:19] op_sel_hi:[1,0,1]
	v_pk_fma_f32 v[20:21], v[202:203], v[52:53], v[20:21] op_sel_hi:[1,0,1]
	v_pk_fma_f32 v[14:15], v[200:201], v[62:63], v[14:15] op_sel_hi:[1,0,1]
	v_pk_fma_f32 v[16:17], v[202:203], v[62:63], v[16:17] op_sel_hi:[1,0,1]
	v_pk_fma_f32 v[10:11], v[200:201], v[64:65], v[10:11] op_sel_hi:[1,0,1]
	v_pk_fma_f32 v[12:13], v[202:203], v[64:65], v[12:13] op_sel_hi:[1,0,1]
	v_pk_fma_f32 v[6:7], v[200:201], v[66:67], v[6:7] op_sel_hi:[1,0,1]
	v_pk_fma_f32 v[8:9], v[202:203], v[66:67], v[8:9] op_sel_hi:[1,0,1]
	v_pk_fma_f32 v[2:3], v[200:201], v[68:69], v[2:3] op_sel_hi:[1,0,1]
	v_pk_fma_f32 v[4:5], v[202:203], v[68:69], v[4:5] op_sel_hi:[1,0,1]
	s_waitcnt vmcnt(8)
	v_pk_fma_f32 v[18:19], v[204:205], v[72:73], v[18:19] op_sel_hi:[1,0,1]
	v_pk_fma_f32 v[20:21], v[206:207], v[72:73], v[20:21] op_sel_hi:[1,0,1]
	v_pk_fma_f32 v[14:15], v[204:205], v[82:83], v[14:15] op_sel_hi:[1,0,1]
	v_pk_fma_f32 v[16:17], v[206:207], v[82:83], v[16:17] op_sel_hi:[1,0,1]
	v_pk_fma_f32 v[10:11], v[204:205], v[84:85], v[10:11] op_sel_hi:[1,0,1]
	v_pk_fma_f32 v[12:13], v[206:207], v[84:85], v[12:13] op_sel_hi:[1,0,1]
	v_pk_fma_f32 v[6:7], v[204:205], v[86:87], v[6:7] op_sel_hi:[1,0,1]
	v_pk_fma_f32 v[8:9], v[206:207], v[86:87], v[8:9] op_sel_hi:[1,0,1]
	v_pk_fma_f32 v[2:3], v[204:205], v[88:89], v[2:3] op_sel_hi:[1,0,1]
	v_pk_fma_f32 v[4:5], v[206:207], v[88:89], v[4:5] op_sel_hi:[1,0,1]
	s_mov_b32 s8, 0xc00000
	v_lshl_add_u64 v[226:227], v[30:31], 0, s[8:9]
	s_add_u32 s4, s8, s12
	v_lshl_add_u64 v[228:229], v[30:31], 0, s[4:5]
	global_load_dwordx4 v[192:195], v[226:227], off
	s_add_u32 s4, s8, s13
	v_lshl_add_u64 v[230:231], v[30:31], 0, s[4:5]
	global_load_dwordx4 v[196:199], v[228:229], off
	s_add_u32 s4, s8, s14
	v_lshl_add_u64 v[232:233], v[30:31], 0, s[4:5]
	global_load_dwordx4 v[200:203], v[230:231], off
	global_load_dwordx4 v[204:207], v[232:233], off
	v_add_u32_e32 v33, 0x1000, v26
	v_add_u32_e32 v64, 0x2000, v26
	ds_read2_b32 v[50:51], v26 offset1:32
	v_add_u32_e32 v66, 0x3000, v26
	v_add_u32_e32 v68, 0x4000, v26
	ds_read2_b32 v[52:53], v26 offset0:64 offset1:96
	ds_read2_b32 v[54:55], v33 offset1:32
	ds_read2_b32 v[56:57], v64 offset1:32
	ds_read2_b32 v[58:59], v66 offset1:32
	ds_read2_b32 v[60:61], v68 offset1:32
	ds_read2_b32 v[62:63], v33 offset0:64 offset1:96
	ds_read2_b32 v[64:65], v64 offset0:64 offset1:96
	ds_read2_b32 v[66:67], v66 offset0:64 offset1:96
	ds_read2_b32 v[68:69], v68 offset0:64 offset1:96
	s_waitcnt lgkmcnt(9)
	v_mov_b32_e32 v70, v51
	s_waitcnt lgkmcnt(7)
	v_mov_b32_e32 v74, v55
	s_waitcnt lgkmcnt(6)
	v_mov_b32_e32 v76, v57
	s_waitcnt lgkmcnt(5)
	v_mov_b32_e32 v78, v59
	s_waitcnt lgkmcnt(4)
	v_mov_b32_e32 v80, v61
	v_mov_b32_e32 v72, v53
	s_waitcnt lgkmcnt(3)
	v_mov_b32_e32 v82, v63
	s_waitcnt lgkmcnt(2)
	v_mov_b32_e32 v84, v65
	s_waitcnt lgkmcnt(1)
	v_mov_b32_e32 v86, v67
	s_waitcnt lgkmcnt(0)
	v_mov_b32_e32 v88, v69
	v_add_u32_e32 v26, 0x200, v26
	s_waitcnt vmcnt(11)
	v_pk_fma_f32 v[18:19], v[208:209], v[50:51], v[18:19] op_sel_hi:[1,0,1]
	v_pk_fma_f32 v[20:21], v[210:211], v[50:51], v[20:21] op_sel_hi:[1,0,1]
	v_pk_fma_f32 v[14:15], v[208:209], v[54:55], v[14:15] op_sel_hi:[1,0,1]
	v_pk_fma_f32 v[16:17], v[210:211], v[54:55], v[16:17] op_sel_hi:[1,0,1]
	v_pk_fma_f32 v[10:11], v[208:209], v[56:57], v[10:11] op_sel_hi:[1,0,1]
	v_pk_fma_f32 v[12:13], v[210:211], v[56:57], v[12:13] op_sel_hi:[1,0,1]
	v_pk_fma_f32 v[6:7], v[208:209], v[58:59], v[6:7] op_sel_hi:[1,0,1]
	v_pk_fma_f32 v[8:9], v[210:211], v[58:59], v[8:9] op_sel_hi:[1,0,1]
	v_pk_fma_f32 v[2:3], v[208:209], v[60:61], v[2:3] op_sel_hi:[1,0,1]
	v_pk_fma_f32 v[4:5], v[210:211], v[60:61], v[4:5] op_sel_hi:[1,0,1]
	s_waitcnt vmcnt(10)
	v_pk_fma_f32 v[18:19], v[212:213], v[70:71], v[18:19] op_sel_hi:[1,0,1]
	v_pk_fma_f32 v[20:21], v[214:215], v[70:71], v[20:21] op_sel_hi:[1,0,1]
	v_pk_fma_f32 v[14:15], v[212:213], v[74:75], v[14:15] op_sel_hi:[1,0,1]
	v_pk_fma_f32 v[16:17], v[214:215], v[74:75], v[16:17] op_sel_hi:[1,0,1]
	v_pk_fma_f32 v[10:11], v[212:213], v[76:77], v[10:11] op_sel_hi:[1,0,1]
	v_pk_fma_f32 v[12:13], v[214:215], v[76:77], v[12:13] op_sel_hi:[1,0,1]
	v_pk_fma_f32 v[6:7], v[212:213], v[78:79], v[6:7] op_sel_hi:[1,0,1]
	v_pk_fma_f32 v[8:9], v[214:215], v[78:79], v[8:9] op_sel_hi:[1,0,1]
	v_pk_fma_f32 v[2:3], v[212:213], v[80:81], v[2:3] op_sel_hi:[1,0,1]
	v_pk_fma_f32 v[4:5], v[214:215], v[80:81], v[4:5] op_sel_hi:[1,0,1]
	s_waitcnt vmcnt(9)
	v_pk_fma_f32 v[18:19], v[216:217], v[52:53], v[18:19] op_sel_hi:[1,0,1]
	v_pk_fma_f32 v[20:21], v[218:219], v[52:53], v[20:21] op_sel_hi:[1,0,1]
	v_pk_fma_f32 v[14:15], v[216:217], v[62:63], v[14:15] op_sel_hi:[1,0,1]
	v_pk_fma_f32 v[16:17], v[218:219], v[62:63], v[16:17] op_sel_hi:[1,0,1]
	v_pk_fma_f32 v[10:11], v[216:217], v[64:65], v[10:11] op_sel_hi:[1,0,1]
	v_pk_fma_f32 v[12:13], v[218:219], v[64:65], v[12:13] op_sel_hi:[1,0,1]
	v_pk_fma_f32 v[6:7], v[216:217], v[66:67], v[6:7] op_sel_hi:[1,0,1]
	v_pk_fma_f32 v[8:9], v[218:219], v[66:67], v[8:9] op_sel_hi:[1,0,1]
	v_pk_fma_f32 v[2:3], v[216:217], v[68:69], v[2:3] op_sel_hi:[1,0,1]
	v_pk_fma_f32 v[4:5], v[218:219], v[68:69], v[4:5] op_sel_hi:[1,0,1]
	s_waitcnt vmcnt(8)
	v_pk_fma_f32 v[18:19], v[220:221], v[72:73], v[18:19] op_sel_hi:[1,0,1]
	v_pk_fma_f32 v[20:21], v[222:223], v[72:73], v[20:21] op_sel_hi:[1,0,1]
	v_pk_fma_f32 v[14:15], v[220:221], v[82:83], v[14:15] op_sel_hi:[1,0,1]
	v_pk_fma_f32 v[16:17], v[222:223], v[82:83], v[16:17] op_sel_hi:[1,0,1]
	v_pk_fma_f32 v[10:11], v[220:221], v[84:85], v[10:11] op_sel_hi:[1,0,1]
	v_pk_fma_f32 v[12:13], v[222:223], v[84:85], v[12:13] op_sel_hi:[1,0,1]
	v_pk_fma_f32 v[6:7], v[220:221], v[86:87], v[6:7] op_sel_hi:[1,0,1]
	v_pk_fma_f32 v[8:9], v[222:223], v[86:87], v[8:9] op_sel_hi:[1,0,1]
	v_pk_fma_f32 v[2:3], v[220:221], v[88:89], v[2:3] op_sel_hi:[1,0,1]
	v_pk_fma_f32 v[4:5], v[222:223], v[88:89], v[4:5] op_sel_hi:[1,0,1]
	s_mov_b32 s8, 0xf00000
	v_lshl_add_u64 v[226:227], v[30:31], 0, s[8:9]
	s_add_u32 s4, s8, s12
	v_lshl_add_u64 v[228:229], v[30:31], 0, s[4:5]
	global_load_dwordx4 v[208:211], v[226:227], off
	s_add_u32 s4, s8, s13
	v_lshl_add_u64 v[230:231], v[30:31], 0, s[4:5]
	global_load_dwordx4 v[212:215], v[228:229], off
	s_add_u32 s4, s8, s14
	v_lshl_add_u64 v[232:233], v[30:31], 0, s[4:5]
	global_load_dwordx4 v[216:219], v[230:231], off
	global_load_dwordx4 v[220:223], v[232:233], off
	v_add_u32_e32 v33, 0x1000, v26
	v_add_u32_e32 v64, 0x2000, v26
	ds_read2_b32 v[50:51], v26 offset1:32
	v_add_u32_e32 v66, 0x3000, v26
	v_add_u32_e32 v68, 0x4000, v26
	ds_read2_b32 v[52:53], v26 offset0:64 offset1:96
	ds_read2_b32 v[54:55], v33 offset1:32
	ds_read2_b32 v[56:57], v64 offset1:32
	ds_read2_b32 v[58:59], v66 offset1:32
	ds_read2_b32 v[60:61], v68 offset1:32
	ds_read2_b32 v[62:63], v33 offset0:64 offset1:96
	ds_read2_b32 v[64:65], v64 offset0:64 offset1:96
	ds_read2_b32 v[66:67], v66 offset0:64 offset1:96
	ds_read2_b32 v[68:69], v68 offset0:64 offset1:96
	s_waitcnt lgkmcnt(9)
	v_mov_b32_e32 v70, v51
	s_waitcnt lgkmcnt(7)
	v_mov_b32_e32 v74, v55
	s_waitcnt lgkmcnt(6)
	v_mov_b32_e32 v76, v57
	s_waitcnt lgkmcnt(5)
	v_mov_b32_e32 v78, v59
	s_waitcnt lgkmcnt(4)
	v_mov_b32_e32 v80, v61
	v_mov_b32_e32 v72, v53
	s_waitcnt lgkmcnt(3)
	v_mov_b32_e32 v82, v63
	s_waitcnt lgkmcnt(2)
	v_mov_b32_e32 v84, v65
	s_waitcnt lgkmcnt(1)
	v_mov_b32_e32 v86, v67
	s_waitcnt lgkmcnt(0)
	v_mov_b32_e32 v88, v69
	v_add_u32_e32 v26, 0x200, v26
	s_waitcnt vmcnt(11)
	v_pk_fma_f32 v[18:19], v[34:35], v[50:51], v[18:19] op_sel_hi:[1,0,1]
	v_pk_fma_f32 v[20:21], v[36:37], v[50:51], v[20:21] op_sel_hi:[1,0,1]
	v_pk_fma_f32 v[14:15], v[34:35], v[54:55], v[14:15] op_sel_hi:[1,0,1]
	v_pk_fma_f32 v[16:17], v[36:37], v[54:55], v[16:17] op_sel_hi:[1,0,1]
	v_pk_fma_f32 v[10:11], v[34:35], v[56:57], v[10:11] op_sel_hi:[1,0,1]
	v_pk_fma_f32 v[12:13], v[36:37], v[56:57], v[12:13] op_sel_hi:[1,0,1]
	v_pk_fma_f32 v[6:7], v[34:35], v[58:59], v[6:7] op_sel_hi:[1,0,1]
	v_pk_fma_f32 v[8:9], v[36:37], v[58:59], v[8:9] op_sel_hi:[1,0,1]
	v_pk_fma_f32 v[2:3], v[34:35], v[60:61], v[2:3] op_sel_hi:[1,0,1]
	v_pk_fma_f32 v[4:5], v[36:37], v[60:61], v[4:5] op_sel_hi:[1,0,1]
	s_waitcnt vmcnt(10)
	v_pk_fma_f32 v[18:19], v[38:39], v[70:71], v[18:19] op_sel_hi:[1,0,1]
	v_pk_fma_f32 v[20:21], v[40:41], v[70:71], v[20:21] op_sel_hi:[1,0,1]
	v_pk_fma_f32 v[14:15], v[38:39], v[74:75], v[14:15] op_sel_hi:[1,0,1]
	v_pk_fma_f32 v[16:17], v[40:41], v[74:75], v[16:17] op_sel_hi:[1,0,1]
	v_pk_fma_f32 v[10:11], v[38:39], v[76:77], v[10:11] op_sel_hi:[1,0,1]
	v_pk_fma_f32 v[12:13], v[40:41], v[76:77], v[12:13] op_sel_hi:[1,0,1]
	v_pk_fma_f32 v[6:7], v[38:39], v[78:79], v[6:7] op_sel_hi:[1,0,1]
	v_pk_fma_f32 v[8:9], v[40:41], v[78:79], v[8:9] op_sel_hi:[1,0,1]
	v_pk_fma_f32 v[2:3], v[38:39], v[80:81], v[2:3] op_sel_hi:[1,0,1]
	v_pk_fma_f32 v[4:5], v[40:41], v[80:81], v[4:5] op_sel_hi:[1,0,1]
	s_waitcnt vmcnt(9)
	v_pk_fma_f32 v[18:19], v[42:43], v[52:53], v[18:19] op_sel_hi:[1,0,1]
	v_pk_fma_f32 v[20:21], v[44:45], v[52:53], v[20:21] op_sel_hi:[1,0,1]
	v_pk_fma_f32 v[14:15], v[42:43], v[62:63], v[14:15] op_sel_hi:[1,0,1]
	v_pk_fma_f32 v[16:17], v[44:45], v[62:63], v[16:17] op_sel_hi:[1,0,1]
	v_pk_fma_f32 v[10:11], v[42:43], v[64:65], v[10:11] op_sel_hi:[1,0,1]
	v_pk_fma_f32 v[12:13], v[44:45], v[64:65], v[12:13] op_sel_hi:[1,0,1]
	v_pk_fma_f32 v[6:7], v[42:43], v[66:67], v[6:7] op_sel_hi:[1,0,1]
	v_pk_fma_f32 v[8:9], v[44:45], v[66:67], v[8:9] op_sel_hi:[1,0,1]
	v_pk_fma_f32 v[2:3], v[42:43], v[68:69], v[2:3] op_sel_hi:[1,0,1]
	v_pk_fma_f32 v[4:5], v[44:45], v[68:69], v[4:5] op_sel_hi:[1,0,1]
	s_waitcnt vmcnt(8)
	v_pk_fma_f32 v[18:19], v[46:47], v[72:73], v[18:19] op_sel_hi:[1,0,1]
	v_pk_fma_f32 v[20:21], v[48:49], v[72:73], v[20:21] op_sel_hi:[1,0,1]
	v_pk_fma_f32 v[14:15], v[46:47], v[82:83], v[14:15] op_sel_hi:[1,0,1]
	v_pk_fma_f32 v[16:17], v[48:49], v[82:83], v[16:17] op_sel_hi:[1,0,1]
	v_pk_fma_f32 v[10:11], v[46:47], v[84:85], v[10:11] op_sel_hi:[1,0,1]
	v_pk_fma_f32 v[12:13], v[48:49], v[84:85], v[12:13] op_sel_hi:[1,0,1]
	v_pk_fma_f32 v[6:7], v[46:47], v[86:87], v[6:7] op_sel_hi:[1,0,1]
	v_pk_fma_f32 v[8:9], v[48:49], v[86:87], v[8:9] op_sel_hi:[1,0,1]
	v_pk_fma_f32 v[2:3], v[46:47], v[88:89], v[2:3] op_sel_hi:[1,0,1]
	v_pk_fma_f32 v[4:5], v[48:49], v[88:89], v[4:5] op_sel_hi:[1,0,1]
	s_mov_b32 s8, 0x1200000
	v_lshl_add_u64 v[226:227], v[30:31], 0, s[8:9]
	s_add_u32 s4, s8, s12
	v_lshl_add_u64 v[228:229], v[30:31], 0, s[4:5]
	global_load_dwordx4 v[34:37], v[226:227], off
	s_add_u32 s4, s8, s13
	v_lshl_add_u64 v[230:231], v[30:31], 0, s[4:5]
	global_load_dwordx4 v[38:41], v[228:229], off
	s_add_u32 s4, s8, s14
	v_lshl_add_u64 v[232:233], v[30:31], 0, s[4:5]
	global_load_dwordx4 v[42:45], v[230:231], off
	global_load_dwordx4 v[46:49], v[232:233], off
	v_add_u32_e32 v33, 0x1000, v26
	v_add_u32_e32 v64, 0x2000, v26
	ds_read2_b32 v[50:51], v26 offset1:32
	v_add_u32_e32 v66, 0x3000, v26
	v_add_u32_e32 v68, 0x4000, v26
	ds_read2_b32 v[52:53], v26 offset0:64 offset1:96
	ds_read2_b32 v[54:55], v33 offset1:32
	ds_read2_b32 v[56:57], v64 offset1:32
	ds_read2_b32 v[58:59], v66 offset1:32
	ds_read2_b32 v[60:61], v68 offset1:32
	ds_read2_b32 v[62:63], v33 offset0:64 offset1:96
	ds_read2_b32 v[64:65], v64 offset0:64 offset1:96
	ds_read2_b32 v[66:67], v66 offset0:64 offset1:96
	ds_read2_b32 v[68:69], v68 offset0:64 offset1:96
	s_waitcnt lgkmcnt(9)
	v_mov_b32_e32 v70, v51
	s_waitcnt lgkmcnt(7)
	v_mov_b32_e32 v74, v55
	s_waitcnt lgkmcnt(6)
	v_mov_b32_e32 v76, v57
	s_waitcnt lgkmcnt(5)
	v_mov_b32_e32 v78, v59
	s_waitcnt lgkmcnt(4)
	v_mov_b32_e32 v80, v61
	v_mov_b32_e32 v72, v53
	s_waitcnt lgkmcnt(3)
	v_mov_b32_e32 v82, v63
	s_waitcnt lgkmcnt(2)
	v_mov_b32_e32 v84, v65
	s_waitcnt lgkmcnt(1)
	v_mov_b32_e32 v86, v67
	s_waitcnt lgkmcnt(0)
	v_mov_b32_e32 v88, v69
	v_add_u32_e32 v26, 0x200, v26
	s_waitcnt vmcnt(11)
	v_pk_fma_f32 v[18:19], v[192:193], v[50:51], v[18:19] op_sel_hi:[1,0,1]
	v_pk_fma_f32 v[20:21], v[194:195], v[50:51], v[20:21] op_sel_hi:[1,0,1]
	v_pk_fma_f32 v[14:15], v[192:193], v[54:55], v[14:15] op_sel_hi:[1,0,1]
	v_pk_fma_f32 v[16:17], v[194:195], v[54:55], v[16:17] op_sel_hi:[1,0,1]
	v_pk_fma_f32 v[10:11], v[192:193], v[56:57], v[10:11] op_sel_hi:[1,0,1]
	v_pk_fma_f32 v[12:13], v[194:195], v[56:57], v[12:13] op_sel_hi:[1,0,1]
	v_pk_fma_f32 v[6:7], v[192:193], v[58:59], v[6:7] op_sel_hi:[1,0,1]
	v_pk_fma_f32 v[8:9], v[194:195], v[58:59], v[8:9] op_sel_hi:[1,0,1]
	v_pk_fma_f32 v[2:3], v[192:193], v[60:61], v[2:3] op_sel_hi:[1,0,1]
	v_pk_fma_f32 v[4:5], v[194:195], v[60:61], v[4:5] op_sel_hi:[1,0,1]
	s_waitcnt vmcnt(10)
	v_pk_fma_f32 v[18:19], v[196:197], v[70:71], v[18:19] op_sel_hi:[1,0,1]
	v_pk_fma_f32 v[20:21], v[198:199], v[70:71], v[20:21] op_sel_hi:[1,0,1]
	v_pk_fma_f32 v[14:15], v[196:197], v[74:75], v[14:15] op_sel_hi:[1,0,1]
	v_pk_fma_f32 v[16:17], v[198:199], v[74:75], v[16:17] op_sel_hi:[1,0,1]
	v_pk_fma_f32 v[10:11], v[196:197], v[76:77], v[10:11] op_sel_hi:[1,0,1]
	v_pk_fma_f32 v[12:13], v[198:199], v[76:77], v[12:13] op_sel_hi:[1,0,1]
	v_pk_fma_f32 v[6:7], v[196:197], v[78:79], v[6:7] op_sel_hi:[1,0,1]
	v_pk_fma_f32 v[8:9], v[198:199], v[78:79], v[8:9] op_sel_hi:[1,0,1]
	v_pk_fma_f32 v[2:3], v[196:197], v[80:81], v[2:3] op_sel_hi:[1,0,1]
	v_pk_fma_f32 v[4:5], v[198:199], v[80:81], v[4:5] op_sel_hi:[1,0,1]
	s_waitcnt vmcnt(9)
	v_pk_fma_f32 v[18:19], v[200:201], v[52:53], v[18:19] op_sel_hi:[1,0,1]
	v_pk_fma_f32 v[20:21], v[202:203], v[52:53], v[20:21] op_sel_hi:[1,0,1]
	v_pk_fma_f32 v[14:15], v[200:201], v[62:63], v[14:15] op_sel_hi:[1,0,1]
	v_pk_fma_f32 v[16:17], v[202:203], v[62:63], v[16:17] op_sel_hi:[1,0,1]
	v_pk_fma_f32 v[10:11], v[200:201], v[64:65], v[10:11] op_sel_hi:[1,0,1]
	v_pk_fma_f32 v[12:13], v[202:203], v[64:65], v[12:13] op_sel_hi:[1,0,1]
	v_pk_fma_f32 v[6:7], v[200:201], v[66:67], v[6:7] op_sel_hi:[1,0,1]
	v_pk_fma_f32 v[8:9], v[202:203], v[66:67], v[8:9] op_sel_hi:[1,0,1]
	v_pk_fma_f32 v[2:3], v[200:201], v[68:69], v[2:3] op_sel_hi:[1,0,1]
	v_pk_fma_f32 v[4:5], v[202:203], v[68:69], v[4:5] op_sel_hi:[1,0,1]
	s_waitcnt vmcnt(8)
	v_pk_fma_f32 v[18:19], v[204:205], v[72:73], v[18:19] op_sel_hi:[1,0,1]
	v_pk_fma_f32 v[20:21], v[206:207], v[72:73], v[20:21] op_sel_hi:[1,0,1]
	v_pk_fma_f32 v[14:15], v[204:205], v[82:83], v[14:15] op_sel_hi:[1,0,1]
	v_pk_fma_f32 v[16:17], v[206:207], v[82:83], v[16:17] op_sel_hi:[1,0,1]
	v_pk_fma_f32 v[10:11], v[204:205], v[84:85], v[10:11] op_sel_hi:[1,0,1]
	v_pk_fma_f32 v[12:13], v[206:207], v[84:85], v[12:13] op_sel_hi:[1,0,1]
	v_pk_fma_f32 v[6:7], v[204:205], v[86:87], v[6:7] op_sel_hi:[1,0,1]
	v_pk_fma_f32 v[8:9], v[206:207], v[86:87], v[8:9] op_sel_hi:[1,0,1]
	v_pk_fma_f32 v[2:3], v[204:205], v[88:89], v[2:3] op_sel_hi:[1,0,1]
	v_pk_fma_f32 v[4:5], v[206:207], v[88:89], v[4:5] op_sel_hi:[1,0,1]
	s_mov_b32 s8, 0x1500000
	v_lshl_add_u64 v[226:227], v[30:31], 0, s[8:9]
	s_add_u32 s4, s8, s12
	v_lshl_add_u64 v[228:229], v[30:31], 0, s[4:5]
	global_load_dwordx4 v[192:195], v[226:227], off
	s_add_u32 s4, s8, s13
	v_lshl_add_u64 v[230:231], v[30:31], 0, s[4:5]
	global_load_dwordx4 v[196:199], v[228:229], off
	s_add_u32 s4, s8, s14
	v_lshl_add_u64 v[232:233], v[30:31], 0, s[4:5]
	global_load_dwordx4 v[200:203], v[230:231], off
	global_load_dwordx4 v[204:207], v[232:233], off
	v_add_u32_e32 v33, 0x1000, v26
	v_add_u32_e32 v64, 0x2000, v26
	ds_read2_b32 v[50:51], v26 offset1:32
	v_add_u32_e32 v66, 0x3000, v26
	v_add_u32_e32 v68, 0x4000, v26
	ds_read2_b32 v[52:53], v26 offset0:64 offset1:96
	ds_read2_b32 v[54:55], v33 offset1:32
	ds_read2_b32 v[56:57], v64 offset1:32
	ds_read2_b32 v[58:59], v66 offset1:32
	ds_read2_b32 v[60:61], v68 offset1:32
	ds_read2_b32 v[62:63], v33 offset0:64 offset1:96
	ds_read2_b32 v[64:65], v64 offset0:64 offset1:96
	ds_read2_b32 v[66:67], v66 offset0:64 offset1:96
	ds_read2_b32 v[68:69], v68 offset0:64 offset1:96
	s_waitcnt lgkmcnt(9)
	v_mov_b32_e32 v70, v51
	s_waitcnt lgkmcnt(7)
	v_mov_b32_e32 v74, v55
	s_waitcnt lgkmcnt(6)
	v_mov_b32_e32 v76, v57
	s_waitcnt lgkmcnt(5)
	v_mov_b32_e32 v78, v59
	s_waitcnt lgkmcnt(4)
	v_mov_b32_e32 v80, v61
	v_mov_b32_e32 v72, v53
	s_waitcnt lgkmcnt(3)
	v_mov_b32_e32 v82, v63
	s_waitcnt lgkmcnt(2)
	v_mov_b32_e32 v84, v65
	s_waitcnt lgkmcnt(1)
	v_mov_b32_e32 v86, v67
	s_waitcnt lgkmcnt(0)
	v_mov_b32_e32 v88, v69
	v_add_u32_e32 v26, 0x200, v26
	s_waitcnt vmcnt(11)
	v_pk_fma_f32 v[18:19], v[208:209], v[50:51], v[18:19] op_sel_hi:[1,0,1]
	v_pk_fma_f32 v[20:21], v[210:211], v[50:51], v[20:21] op_sel_hi:[1,0,1]
	v_pk_fma_f32 v[14:15], v[208:209], v[54:55], v[14:15] op_sel_hi:[1,0,1]
	v_pk_fma_f32 v[16:17], v[210:211], v[54:55], v[16:17] op_sel_hi:[1,0,1]
	v_pk_fma_f32 v[10:11], v[208:209], v[56:57], v[10:11] op_sel_hi:[1,0,1]
	v_pk_fma_f32 v[12:13], v[210:211], v[56:57], v[12:13] op_sel_hi:[1,0,1]
	v_pk_fma_f32 v[6:7], v[208:209], v[58:59], v[6:7] op_sel_hi:[1,0,1]
	v_pk_fma_f32 v[8:9], v[210:211], v[58:59], v[8:9] op_sel_hi:[1,0,1]
	v_pk_fma_f32 v[2:3], v[208:209], v[60:61], v[2:3] op_sel_hi:[1,0,1]
	v_pk_fma_f32 v[4:5], v[210:211], v[60:61], v[4:5] op_sel_hi:[1,0,1]
	s_waitcnt vmcnt(10)
	v_pk_fma_f32 v[18:19], v[212:213], v[70:71], v[18:19] op_sel_hi:[1,0,1]
	v_pk_fma_f32 v[20:21], v[214:215], v[70:71], v[20:21] op_sel_hi:[1,0,1]
	v_pk_fma_f32 v[14:15], v[212:213], v[74:75], v[14:15] op_sel_hi:[1,0,1]
	v_pk_fma_f32 v[16:17], v[214:215], v[74:75], v[16:17] op_sel_hi:[1,0,1]
	v_pk_fma_f32 v[10:11], v[212:213], v[76:77], v[10:11] op_sel_hi:[1,0,1]
	v_pk_fma_f32 v[12:13], v[214:215], v[76:77], v[12:13] op_sel_hi:[1,0,1]
	v_pk_fma_f32 v[6:7], v[212:213], v[78:79], v[6:7] op_sel_hi:[1,0,1]
	v_pk_fma_f32 v[8:9], v[214:215], v[78:79], v[8:9] op_sel_hi:[1,0,1]
	v_pk_fma_f32 v[2:3], v[212:213], v[80:81], v[2:3] op_sel_hi:[1,0,1]
	v_pk_fma_f32 v[4:5], v[214:215], v[80:81], v[4:5] op_sel_hi:[1,0,1]
	s_waitcnt vmcnt(9)
	v_pk_fma_f32 v[18:19], v[216:217], v[52:53], v[18:19] op_sel_hi:[1,0,1]
	v_pk_fma_f32 v[20:21], v[218:219], v[52:53], v[20:21] op_sel_hi:[1,0,1]
	v_pk_fma_f32 v[14:15], v[216:217], v[62:63], v[14:15] op_sel_hi:[1,0,1]
	v_pk_fma_f32 v[16:17], v[218:219], v[62:63], v[16:17] op_sel_hi:[1,0,1]
	v_pk_fma_f32 v[10:11], v[216:217], v[64:65], v[10:11] op_sel_hi:[1,0,1]
	v_pk_fma_f32 v[12:13], v[218:219], v[64:65], v[12:13] op_sel_hi:[1,0,1]
	v_pk_fma_f32 v[6:7], v[216:217], v[66:67], v[6:7] op_sel_hi:[1,0,1]
	v_pk_fma_f32 v[8:9], v[218:219], v[66:67], v[8:9] op_sel_hi:[1,0,1]
	v_pk_fma_f32 v[2:3], v[216:217], v[68:69], v[2:3] op_sel_hi:[1,0,1]
	v_pk_fma_f32 v[4:5], v[218:219], v[68:69], v[4:5] op_sel_hi:[1,0,1]
	s_waitcnt vmcnt(8)
	v_pk_fma_f32 v[18:19], v[220:221], v[72:73], v[18:19] op_sel_hi:[1,0,1]
	v_pk_fma_f32 v[20:21], v[222:223], v[72:73], v[20:21] op_sel_hi:[1,0,1]
	v_pk_fma_f32 v[14:15], v[220:221], v[82:83], v[14:15] op_sel_hi:[1,0,1]
	v_pk_fma_f32 v[16:17], v[222:223], v[82:83], v[16:17] op_sel_hi:[1,0,1]
	v_pk_fma_f32 v[10:11], v[220:221], v[84:85], v[10:11] op_sel_hi:[1,0,1]
	v_pk_fma_f32 v[12:13], v[222:223], v[84:85], v[12:13] op_sel_hi:[1,0,1]
	v_pk_fma_f32 v[6:7], v[220:221], v[86:87], v[6:7] op_sel_hi:[1,0,1]
	v_pk_fma_f32 v[8:9], v[222:223], v[86:87], v[8:9] op_sel_hi:[1,0,1]
	v_pk_fma_f32 v[2:3], v[220:221], v[88:89], v[2:3] op_sel_hi:[1,0,1]
	v_pk_fma_f32 v[4:5], v[222:223], v[88:89], v[4:5] op_sel_hi:[1,0,1]
	v_add_u32_e32 v33, 0x1000, v26
	v_add_u32_e32 v64, 0x2000, v26
	ds_read2_b32 v[50:51], v26 offset1:32
	v_add_u32_e32 v66, 0x3000, v26
	v_add_u32_e32 v68, 0x4000, v26
	ds_read2_b32 v[52:53], v26 offset0:64 offset1:96
	ds_read2_b32 v[54:55], v33 offset1:32
	ds_read2_b32 v[56:57], v64 offset1:32
	ds_read2_b32 v[58:59], v66 offset1:32
	ds_read2_b32 v[60:61], v68 offset1:32
	ds_read2_b32 v[62:63], v33 offset0:64 offset1:96
	ds_read2_b32 v[64:65], v64 offset0:64 offset1:96
	ds_read2_b32 v[66:67], v66 offset0:64 offset1:96
	ds_read2_b32 v[68:69], v68 offset0:64 offset1:96
	s_waitcnt lgkmcnt(9)
	v_mov_b32_e32 v70, v51
	s_waitcnt lgkmcnt(7)
	v_mov_b32_e32 v74, v55
	s_waitcnt lgkmcnt(6)
	v_mov_b32_e32 v76, v57
	s_waitcnt lgkmcnt(5)
	v_mov_b32_e32 v78, v59
	s_waitcnt lgkmcnt(4)
	v_mov_b32_e32 v80, v61
	v_mov_b32_e32 v72, v53
	s_waitcnt lgkmcnt(3)
	v_mov_b32_e32 v82, v63
	s_waitcnt lgkmcnt(2)
	v_mov_b32_e32 v84, v65
	s_waitcnt lgkmcnt(1)
	v_mov_b32_e32 v86, v67
	s_waitcnt lgkmcnt(0)
	v_mov_b32_e32 v88, v69
	v_add_u32_e32 v26, 0x200, v26
	s_waitcnt vmcnt(7)
	v_pk_fma_f32 v[18:19], v[34:35], v[50:51], v[18:19] op_sel_hi:[1,0,1]
	v_pk_fma_f32 v[20:21], v[36:37], v[50:51], v[20:21] op_sel_hi:[1,0,1]
	v_pk_fma_f32 v[14:15], v[34:35], v[54:55], v[14:15] op_sel_hi:[1,0,1]
	v_pk_fma_f32 v[16:17], v[36:37], v[54:55], v[16:17] op_sel_hi:[1,0,1]
	v_pk_fma_f32 v[10:11], v[34:35], v[56:57], v[10:11] op_sel_hi:[1,0,1]
	v_pk_fma_f32 v[12:13], v[36:37], v[56:57], v[12:13] op_sel_hi:[1,0,1]
	v_pk_fma_f32 v[6:7], v[34:35], v[58:59], v[6:7] op_sel_hi:[1,0,1]
	v_pk_fma_f32 v[8:9], v[36:37], v[58:59], v[8:9] op_sel_hi:[1,0,1]
	v_pk_fma_f32 v[2:3], v[34:35], v[60:61], v[2:3] op_sel_hi:[1,0,1]
	v_pk_fma_f32 v[4:5], v[36:37], v[60:61], v[4:5] op_sel_hi:[1,0,1]
	s_waitcnt vmcnt(6)
	v_pk_fma_f32 v[18:19], v[38:39], v[70:71], v[18:19] op_sel_hi:[1,0,1]
	v_pk_fma_f32 v[20:21], v[40:41], v[70:71], v[20:21] op_sel_hi:[1,0,1]
	v_pk_fma_f32 v[14:15], v[38:39], v[74:75], v[14:15] op_sel_hi:[1,0,1]
	v_pk_fma_f32 v[16:17], v[40:41], v[74:75], v[16:17] op_sel_hi:[1,0,1]
	v_pk_fma_f32 v[10:11], v[38:39], v[76:77], v[10:11] op_sel_hi:[1,0,1]
	v_pk_fma_f32 v[12:13], v[40:41], v[76:77], v[12:13] op_sel_hi:[1,0,1]
	v_pk_fma_f32 v[6:7], v[38:39], v[78:79], v[6:7] op_sel_hi:[1,0,1]
	v_pk_fma_f32 v[8:9], v[40:41], v[78:79], v[8:9] op_sel_hi:[1,0,1]
	v_pk_fma_f32 v[2:3], v[38:39], v[80:81], v[2:3] op_sel_hi:[1,0,1]
	v_pk_fma_f32 v[4:5], v[40:41], v[80:81], v[4:5] op_sel_hi:[1,0,1]
	s_waitcnt vmcnt(5)
	v_pk_fma_f32 v[18:19], v[42:43], v[52:53], v[18:19] op_sel_hi:[1,0,1]
	v_pk_fma_f32 v[20:21], v[44:45], v[52:53], v[20:21] op_sel_hi:[1,0,1]
	v_pk_fma_f32 v[14:15], v[42:43], v[62:63], v[14:15] op_sel_hi:[1,0,1]
	v_pk_fma_f32 v[16:17], v[44:45], v[62:63], v[16:17] op_sel_hi:[1,0,1]
	v_pk_fma_f32 v[10:11], v[42:43], v[64:65], v[10:11] op_sel_hi:[1,0,1]
	v_pk_fma_f32 v[12:13], v[44:45], v[64:65], v[12:13] op_sel_hi:[1,0,1]
	v_pk_fma_f32 v[6:7], v[42:43], v[66:67], v[6:7] op_sel_hi:[1,0,1]
	v_pk_fma_f32 v[8:9], v[44:45], v[66:67], v[8:9] op_sel_hi:[1,0,1]
	v_pk_fma_f32 v[2:3], v[42:43], v[68:69], v[2:3] op_sel_hi:[1,0,1]
	v_pk_fma_f32 v[4:5], v[44:45], v[68:69], v[4:5] op_sel_hi:[1,0,1]
	s_waitcnt vmcnt(4)
	v_pk_fma_f32 v[18:19], v[46:47], v[72:73], v[18:19] op_sel_hi:[1,0,1]
	v_pk_fma_f32 v[20:21], v[48:49], v[72:73], v[20:21] op_sel_hi:[1,0,1]
	v_pk_fma_f32 v[14:15], v[46:47], v[82:83], v[14:15] op_sel_hi:[1,0,1]
	v_pk_fma_f32 v[16:17], v[48:49], v[82:83], v[16:17] op_sel_hi:[1,0,1]
	v_pk_fma_f32 v[10:11], v[46:47], v[84:85], v[10:11] op_sel_hi:[1,0,1]
	v_pk_fma_f32 v[12:13], v[48:49], v[84:85], v[12:13] op_sel_hi:[1,0,1]
	v_pk_fma_f32 v[6:7], v[46:47], v[86:87], v[6:7] op_sel_hi:[1,0,1]
	v_pk_fma_f32 v[8:9], v[48:49], v[86:87], v[8:9] op_sel_hi:[1,0,1]
	v_pk_fma_f32 v[2:3], v[46:47], v[88:89], v[2:3] op_sel_hi:[1,0,1]
	v_pk_fma_f32 v[4:5], v[48:49], v[88:89], v[4:5] op_sel_hi:[1,0,1]
	v_add_u32_e32 v33, 0x1000, v26
	v_add_u32_e32 v64, 0x2000, v26
	ds_read2_b32 v[50:51], v26 offset1:32
	v_add_u32_e32 v66, 0x3000, v26
	v_add_u32_e32 v68, 0x4000, v26
	ds_read2_b32 v[52:53], v26 offset0:64 offset1:96
	ds_read2_b32 v[54:55], v33 offset1:32
	ds_read2_b32 v[56:57], v64 offset1:32
	ds_read2_b32 v[58:59], v66 offset1:32
	ds_read2_b32 v[60:61], v68 offset1:32
	ds_read2_b32 v[62:63], v33 offset0:64 offset1:96
	ds_read2_b32 v[64:65], v64 offset0:64 offset1:96
	ds_read2_b32 v[66:67], v66 offset0:64 offset1:96
	ds_read2_b32 v[68:69], v68 offset0:64 offset1:96
	s_waitcnt lgkmcnt(9)
	v_mov_b32_e32 v70, v51
	s_waitcnt lgkmcnt(7)
	v_mov_b32_e32 v74, v55
	s_waitcnt lgkmcnt(6)
	v_mov_b32_e32 v76, v57
	s_waitcnt lgkmcnt(5)
	v_mov_b32_e32 v78, v59
	s_waitcnt lgkmcnt(4)
	v_mov_b32_e32 v80, v61
	v_mov_b32_e32 v72, v53
	s_waitcnt lgkmcnt(3)
	v_mov_b32_e32 v82, v63
	s_waitcnt lgkmcnt(2)
	v_mov_b32_e32 v84, v65
	s_waitcnt lgkmcnt(1)
	v_mov_b32_e32 v86, v67
	s_waitcnt lgkmcnt(0)
	v_mov_b32_e32 v88, v69
	v_add_u32_e32 v26, 0x200, v26
	s_waitcnt vmcnt(3)
	v_pk_fma_f32 v[18:19], v[192:193], v[50:51], v[18:19] op_sel_hi:[1,0,1]
	v_pk_fma_f32 v[20:21], v[194:195], v[50:51], v[20:21] op_sel_hi:[1,0,1]
	v_pk_fma_f32 v[14:15], v[192:193], v[54:55], v[14:15] op_sel_hi:[1,0,1]
	v_pk_fma_f32 v[16:17], v[194:195], v[54:55], v[16:17] op_sel_hi:[1,0,1]
	v_pk_fma_f32 v[10:11], v[192:193], v[56:57], v[10:11] op_sel_hi:[1,0,1]
	v_pk_fma_f32 v[12:13], v[194:195], v[56:57], v[12:13] op_sel_hi:[1,0,1]
	v_pk_fma_f32 v[6:7], v[192:193], v[58:59], v[6:7] op_sel_hi:[1,0,1]
	v_pk_fma_f32 v[8:9], v[194:195], v[58:59], v[8:9] op_sel_hi:[1,0,1]
	v_pk_fma_f32 v[2:3], v[192:193], v[60:61], v[2:3] op_sel_hi:[1,0,1]
	v_pk_fma_f32 v[4:5], v[194:195], v[60:61], v[4:5] op_sel_hi:[1,0,1]
	s_waitcnt vmcnt(2)
	v_pk_fma_f32 v[18:19], v[196:197], v[70:71], v[18:19] op_sel_hi:[1,0,1]
	v_pk_fma_f32 v[20:21], v[198:199], v[70:71], v[20:21] op_sel_hi:[1,0,1]
	v_pk_fma_f32 v[14:15], v[196:197], v[74:75], v[14:15] op_sel_hi:[1,0,1]
	v_pk_fma_f32 v[16:17], v[198:199], v[74:75], v[16:17] op_sel_hi:[1,0,1]
	v_pk_fma_f32 v[10:11], v[196:197], v[76:77], v[10:11] op_sel_hi:[1,0,1]
	v_pk_fma_f32 v[12:13], v[198:199], v[76:77], v[12:13] op_sel_hi:[1,0,1]
	v_pk_fma_f32 v[6:7], v[196:197], v[78:79], v[6:7] op_sel_hi:[1,0,1]
	v_pk_fma_f32 v[8:9], v[198:199], v[78:79], v[8:9] op_sel_hi:[1,0,1]
	v_pk_fma_f32 v[2:3], v[196:197], v[80:81], v[2:3] op_sel_hi:[1,0,1]
	v_pk_fma_f32 v[4:5], v[198:199], v[80:81], v[4:5] op_sel_hi:[1,0,1]
	s_waitcnt vmcnt(1)
	v_pk_fma_f32 v[18:19], v[200:201], v[52:53], v[18:19] op_sel_hi:[1,0,1]
	v_pk_fma_f32 v[20:21], v[202:203], v[52:53], v[20:21] op_sel_hi:[1,0,1]
	v_pk_fma_f32 v[14:15], v[200:201], v[62:63], v[14:15] op_sel_hi:[1,0,1]
	v_pk_fma_f32 v[16:17], v[202:203], v[62:63], v[16:17] op_sel_hi:[1,0,1]
	v_pk_fma_f32 v[10:11], v[200:201], v[64:65], v[10:11] op_sel_hi:[1,0,1]
	v_pk_fma_f32 v[12:13], v[202:203], v[64:65], v[12:13] op_sel_hi:[1,0,1]
	v_pk_fma_f32 v[6:7], v[200:201], v[66:67], v[6:7] op_sel_hi:[1,0,1]
	v_pk_fma_f32 v[8:9], v[202:203], v[66:67], v[8:9] op_sel_hi:[1,0,1]
	v_pk_fma_f32 v[2:3], v[200:201], v[68:69], v[2:3] op_sel_hi:[1,0,1]
	v_pk_fma_f32 v[4:5], v[202:203], v[68:69], v[4:5] op_sel_hi:[1,0,1]
	s_waitcnt vmcnt(0)
	v_pk_fma_f32 v[18:19], v[204:205], v[72:73], v[18:19] op_sel_hi:[1,0,1]
	v_pk_fma_f32 v[20:21], v[206:207], v[72:73], v[20:21] op_sel_hi:[1,0,1]
	v_pk_fma_f32 v[14:15], v[204:205], v[82:83], v[14:15] op_sel_hi:[1,0,1]
	v_pk_fma_f32 v[16:17], v[206:207], v[82:83], v[16:17] op_sel_hi:[1,0,1]
	v_pk_fma_f32 v[10:11], v[204:205], v[84:85], v[10:11] op_sel_hi:[1,0,1]
	v_pk_fma_f32 v[12:13], v[206:207], v[84:85], v[12:13] op_sel_hi:[1,0,1]
	v_pk_fma_f32 v[6:7], v[204:205], v[86:87], v[6:7] op_sel_hi:[1,0,1]
	v_pk_fma_f32 v[8:9], v[206:207], v[86:87], v[8:9] op_sel_hi:[1,0,1]
	v_pk_fma_f32 v[2:3], v[204:205], v[88:89], v[2:3] op_sel_hi:[1,0,1]
	v_pk_fma_f32 v[4:5], v[206:207], v[88:89], v[4:5] op_sel_hi:[1,0,1]
	ds_write_b128 v25, v[18:21] offset:20480
	ds_write_b128 v25, v[14:17] offset:20736
	ds_write_b128 v25, v[10:13] offset:20992
	ds_write_b128 v25, v[6:9] offset:21248
	ds_write_b128 v25, v[2:5] offset:21504
	s_waitcnt lgkmcnt(0)
	s_barrier
	s_and_saveexec_b64 s[4:5], vcc
	s_cbranch_execz .LBB0_117
	s_mov_b32 s8, 5
	ds_read2st64_b32 v[2:3], v32 offset0:80 offset1:85
	ds_read2st64_b32 v[4:5], v32 offset0:90 offset1:95
	ds_read2st64_b32 v[6:7], v32 offset0:100 offset1:105
	ds_read2st64_b32 v[8:9], v32 offset0:110 offset1:115
	ds_read2st64_b32 v[10:11], v32 offset0:120 offset1:125
	ds_read2st64_b32 v[12:13], v32 offset0:130 offset1:135
	ds_read2st64_b32 v[14:15], v32 offset0:140 offset1:145
	ds_read2st64_b32 v[16:17], v32 offset0:150 offset1:155
	ds_read2st64_b32 v[18:19], v32 offset0:160 offset1:165
	ds_read2st64_b32 v[20:21], v32 offset0:170 offset1:175
	ds_read2st64_b32 v[30:31], v32 offset0:180 offset1:185
	ds_read2st64_b32 v[34:35], v32 offset0:190 offset1:195
	ds_read2st64_b32 v[36:37], v32 offset0:200 offset1:205
	ds_read2st64_b32 v[38:39], v32 offset0:210 offset1:215
	ds_read2st64_b32 v[40:41], v32 offset0:220 offset1:225
	ds_read2st64_b32 v[42:43], v32 offset0:230 offset1:235
	s_ashr_i32 s9, s8, 31
	s_lshl_b64 s[8:9], s[8:9], 3
	s_add_u32 s8, s0, s8
	s_addc_u32 s9, s1, s9
	s_load_dwordx2 s[8:9], s[8:9], 0x0
	s_mul_i32 s17, s16, 0x1800
	s_add_i32 s17, s17, s6
	v_or_b32_e32 v44, s17, v24
	v_ashrrev_i32_e32 v45, 31, v44
	s_waitcnt lgkmcnt(0)
	v_lshl_add_u64 v[44:45], v[44:45], 2, s[8:9]
	global_load_dword v33, v[44:45], off
	v_add_f32_e32 v2, 0, v2
	v_add_f32_e32 v2, v2, v3
	v_add_f32_e32 v2, v2, v4
	v_add_f32_e32 v2, v2, v5
	v_add_f32_e32 v2, v2, v6
	v_add_f32_e32 v2, v2, v7
	v_add_f32_e32 v2, v2, v8
	v_add_f32_e32 v2, v2, v9
	v_add_f32_e32 v2, v2, v10
	v_add_f32_e32 v2, v2, v11
	v_add_f32_e32 v2, v2, v12
	v_add_f32_e32 v2, v2, v13
	v_add_f32_e32 v2, v2, v14
	v_add_f32_e32 v2, v2, v15
	v_add_f32_e32 v2, v2, v16
	v_add_f32_e32 v2, v2, v17
	v_add_f32_e32 v2, v2, v18
	v_add_f32_e32 v2, v2, v19
	v_add_f32_e32 v2, v2, v20
	v_add_f32_e32 v2, v2, v21
	v_add_f32_e32 v2, v2, v30
	v_add_f32_e32 v2, v2, v31
	v_add_f32_e32 v2, v2, v34
	v_add_f32_e32 v2, v2, v35
	v_add_f32_e32 v2, v2, v36
	v_add_f32_e32 v2, v2, v37
	v_add_f32_e32 v2, v2, v38
	v_add_f32_e32 v2, v2, v39
	v_mad_i64_i32 v[44:45], s[8:9], s16, 5, v[22:23]
	v_mov_b64_e32 v[46:47], s[10:11]
	v_add_f32_e32 v2, v2, v40
	v_mad_u64_u32 v[46:47], s[8:9], v44, s3, v[46:47]
	v_add_f32_e32 v2, v2, v41
	v_mad_i32_i24 v47, v45, s3, v47
	v_add_f32_e32 v2, v2, v42
	v_lshlrev_b32_e32 v26, 2, v24
	v_lshl_add_u64 v[44:45], s[6:7], 2, v[46:47]
	v_add_f32_e32 v2, v2, v43
	s_waitcnt vmcnt(0)
	v_add_f32_e32 v4, v2, v33
	v_lshl_add_u64 v[2:3], v[44:45], 0, v[26:27]
	global_store_dword v[2:3], v4, off
	s_branch .LBB0_117
